# speedup vs baseline: 1.0020x; 1.0020x over previous
_Z11main_kernelPKDv4_jPKfS3_PfPjS4_:
	s_and_b32 s4, s2, 7
	s_ashr_i32 s5, s2, 3
	s_bfe_u32 s3, s2, 0x20001
	s_lshl_b32 s2, s2, 5
	s_and_b32 s2, s2, 32
	s_load_dwordx8 s[16:23], s[0:1], 0x0
	s_add_i32 s2, s2, s5
	s_lshl_b32 s33, s2, 1
	s_lshl_b32 s8, s3, 7
	s_add_i32 s10, s33, s8
	s_mov_b32 s8, s10
	v_and_b32_e32 v194, 63, v0
	v_writelane_b32 v240, s8, 0
	s_mul_i32 s35, s5, 5
	s_mov_b32 s47, 0x20000
	s_mov_b32 s46, 0x400000
	s_waitcnt lgkmcnt(0)
	s_and_b32 s45, s17, 0xffff
	v_writelane_b32 v240, s9, 1
	s_lshl_b32 s8, s10, 13
	s_add_i32 s35, s35, s4
	s_and_b32 s35, s35, 7
	s_and_b32 s97, s4, 1
	s_lshl_b32 s97, s97, 3
	s_or_b32 s35, s35, s97
	s_mov_b32 s4, s16
	s_mov_b32 s5, s45
	s_mov_b32 s6, s46
	s_mov_b32 s7, s47
	v_lshlrev_b32_e32 v195, 4, v194
	s_or_b32 s9, s8, 0x400
	v_lshrrev_b32_e32 v1, 6, v0
	s_nop 0
	v_readfirstlane_b32 s97, v1
	s_lshl_b32 s98, s97, 11
	s_add_i32 s99, s8, s98
	buffer_load_dwordx4 v[34:37], v195, s[4:7], s99 offen
	buffer_load_dwordx4 v[38:41], v195, s[4:7], s99 offen offset:1024
	s_or_b32 s9, s8, 0x800
	v_lshrrev_b32_e32 v1, 6, v0
	s_or_b32 s10, s8, 0xc00
	s_or_b32 s9, s8, 0x1000
	s_and_b32 s12, s35, 15
	s_or_b32 s10, s8, 0x1400
	v_readfirstlane_b32 s52, v1
	s_lshl_b32 s53, s3, 20
	s_lshl_b32 s9, s12, 16
	s_lshl_b32 s95, s52, 13
	s_or_b32 s54, s9, s53
	s_add_i32 s54, s54, s95
	s_or_b32 s55, s54, 0x400
	buffer_load_dwordx4 v[18:21], v195, s[4:7], s54 offen
	buffer_load_dwordx4 v[22:25], v195, s[4:7], s55 offen
	s_or_b32 s9, s8, 0x1800
	s_or_b32 s10, s8, 0x1c00
	s_or_b32 s9, s8, 0x2000
	s_or_b32 s10, s8, 0x2400
	s_or_b32 s9, s8, 0x2800
	s_or_b32 vcc_lo, s54, 0x800
	s_or_b32 s10, s8, 0x2c00
	s_or_b32 vcc_hi, s54, 0xc00
	buffer_load_dwordx4 v[98:101], v195, s[4:7], vcc_lo offen
	buffer_load_dwordx4 v[102:105], v195, s[4:7], vcc_hi offen
	s_or_b32 s9, s8, 0x3000
	s_or_b32 s10, s8, 0x3400
	s_or_b32 s9, s8, 0x3800
	s_or_b32 s34, s54, 0x1000
	s_or_b32 s8, s8, 0x3c00
	s_or_b32 s41, s54, 0x1400
	buffer_load_dwordx4 v[106:109], v195, s[4:7], s34 offen
	buffer_load_dwordx4 v[110:113], v195, s[4:7], s41 offen
	s_lshl_b32 s8, s3, 12
	s_lshl_b32 s9, s2, 6
	v_and_b32_e32 v163, 31, v0
	s_add_i32 s9, s9, s8
	v_or_b32_e32 v2, s9, v163
	v_ashrrev_i32_e32 v3, 31, v2
	v_lshl_add_u64 v[2:3], v[2:3], 2, s[18:19]
	s_or_b32 s60, s54, 0x1800
	global_load_dword v198, v[2:3], off
	global_load_dword v199, v[2:3], off offset:128
	s_or_b32 s61, s54, 0x1c00
	buffer_load_dwordx4 v[114:117], v195, s[4:7], s60 offen
	buffer_load_dwordx4 v[118:121], v195, s[4:7], s61 offen
	s_lshl_b32 s2, s2, 20
	s_lshl_b32 s3, s3, 26
	v_bfe_u32 v196, v0, 5, 1
	s_lshl_b32 s13, s52, 7
	v_lshlrev_b32_e32 v197, 2, v163
	s_add_i32 s62, s2, s3
	s_brev_b32 s38, 8
	s_and_b32 s37, s21, 0xffff
	v_lshl_or_b32 v201, v196, 16, v197
	s_add_i32 s62, s62, s13
	s_mov_b32 s8, s20
	s_mov_b32 s9, s37
	s_mov_b32 s10, s38
	s_mov_b32 s11, s47
	v_lshl_or_b32 v26, s12, 10, v201
	s_add_i32 s70, s62, 0x40000
	s_add_i32 s78, s62, 0x80000
	s_add_i32 s86, s62, 0xc0000
	s_add_i32 s63, s62, 0x4000
	s_add_i32 s64, s62, 0x8000
	s_add_i32 s65, s62, 0xc000
	s_add_i32 s66, s62, 0x20000
	s_add_i32 s67, s62, 0x24000
	s_add_i32 s68, s62, 0x28000
	s_add_i32 s69, s62, 0x2c000
	buffer_load_dword v218, v26, s[8:11], s62 offen nt
	buffer_load_dword v220, v26, s[8:11], s63 offen nt
	buffer_load_dword v222, v26, s[8:11], s64 offen nt
	buffer_load_dword v225, v26, s[8:11], s65 offen nt
	buffer_load_dword v219, v26, s[8:11], s66 offen nt
	buffer_load_dword v221, v26, s[8:11], s67 offen nt
	buffer_load_dword v223, v26, s[8:11], s68 offen nt
	buffer_load_dword v226, v26, s[8:11], s69 offen nt
	s_add_i32 s71, s62, 0x44000
	s_add_i32 s72, s62, 0x48000
	s_add_i32 s73, s62, 0x4c000
	s_add_i32 s74, s62, 0x60000
	s_add_i32 s75, s62, 0x64000
	s_add_i32 s76, s62, 0x68000
	s_add_i32 s77, s62, 0x6c000
	buffer_load_dword v232, v26, s[8:11], s70 offen nt
	buffer_load_dword v233, v26, s[8:11], s71 offen nt
	buffer_load_dword v234, v26, s[8:11], s72 offen nt
	buffer_load_dword v235, v26, s[8:11], s73 offen nt
	buffer_load_dword v228, v26, s[8:11], s74 offen nt
	buffer_load_dword v229, v26, s[8:11], s75 offen nt
	buffer_load_dword v230, v26, s[8:11], s76 offen nt
	buffer_load_dword v231, v26, s[8:11], s77 offen nt
	s_add_i32 s79, s62, 0x84000
	s_add_i32 s80, s62, 0x88000
	s_add_i32 s81, s62, 0x8c000
	s_add_i32 s82, s62, 0xa0000
	s_add_i32 s83, s62, 0xa4000
	s_add_i32 s84, s62, 0xa8000
	s_add_i32 s85, s62, 0xac000
	buffer_load_dword v203, v26, s[8:11], s78 offen nt
	buffer_load_dword v205, v26, s[8:11], s79 offen nt
	buffer_load_dword v207, v26, s[8:11], s80 offen nt
	buffer_load_dword v210, v26, s[8:11], s81 offen nt
	buffer_load_dword v204, v26, s[8:11], s82 offen nt
	buffer_load_dword v206, v26, s[8:11], s83 offen nt
	buffer_load_dword v208, v26, s[8:11], s84 offen nt
	buffer_load_dword v211, v26, s[8:11], s85 offen nt
	s_add_i32 s87, s62, 0xc4000
	s_add_i32 s88, s62, 0xc8000
	s_add_i32 s89, s62, 0xcc000
	s_add_i32 s90, s62, 0xe0000
	s_add_i32 s91, s62, 0xe4000
	s_add_i32 s92, s62, 0xe8000
	s_add_i32 s93, s62, 0xec000
	buffer_load_dword v212, v26, s[8:11], s86 offen nt
	buffer_load_dword v213, v26, s[8:11], s87 offen nt
	buffer_load_dword v214, v26, s[8:11], s88 offen nt
	buffer_load_dword v215, v26, s[8:11], s89 offen nt
	buffer_load_dword v190, v26, s[8:11], s90 offen nt
	buffer_load_dword v192, v26, s[8:11], s91 offen nt
	buffer_load_dword v193, v26, s[8:11], s92 offen nt
	buffer_load_dword v202, v26, s[8:11], s93 offen nt
	s_waitcnt vmcnt(42)
	v_add_u32_e32 v2, s98, v195
	ds_write_b128 v2, v[34:37] offset:40960
	ds_write_b128 v2, v[38:41] offset:41984
	s_waitcnt lgkmcnt(0)
	s_barrier
	ds_read_b128 v[34:37], v195 offset:40960
	ds_read_b128 v[38:41], v195 offset:41984
	ds_read_b128 v[42:45], v195 offset:43008
	ds_read_b128 v[46:49], v195 offset:44032
	ds_read_b128 v[50:53], v195 offset:45056
	ds_read_b128 v[54:57], v195 offset:46080
	ds_read_b128 v[58:61], v195 offset:47104
	ds_read_b128 v[62:65], v195 offset:48128
	ds_read_b128 v[66:69], v195 offset:49152
	ds_read_b128 v[70:73], v195 offset:50176
	ds_read_b128 v[74:77], v195 offset:51200
	ds_read_b128 v[78:81], v195 offset:52224
	ds_read_b128 v[82:85], v195 offset:53248
	ds_read_b128 v[86:89], v195 offset:54272
	ds_read_b128 v[90:93], v195 offset:55296
	ds_read_b128 v[94:97], v195 offset:56320
	v_mov_b32_e32 v236, 0x7f7f7f7f
	s_load_dwordx4 s[0:3], s[0:1], 0x20
	s_mov_b32 s44, s16
	s_waitcnt vmcnt(40)
	s_waitcnt lgkmcnt(0)
	v_mfma_scale_f32_32x32x64_f8f6f4 v[2:17], v[34:41], v[18:25], 0, v236, v236 op_sel_hi:[0,0,0]
	v_lshlrev_b32_e32 v160, 2, v196
	s_mov_b32 s39, s47
	s_waitcnt lgkmcnt(0)
	v_writelane_b32 v240, s0, 2
	s_mov_b32 s94, 0
	v_mov_b32_e32 v162, 0
	v_writelane_b32 v240, s1, 3
	v_writelane_b32 v240, s2, 4
	v_writelane_b32 v240, s3, 5
	v_writelane_b32 v240, s16, 6
	s_mov_b32 s36, s20
	v_sub_u32_e32 v26, v163, v160
	v_writelane_b32 v240, s17, 7
	v_writelane_b32 v240, s18, 8
	v_writelane_b32 v240, s19, 9
	v_writelane_b32 v240, s20, 10
	s_waitcnt vmcnt(38)
	v_mfma_scale_f32_32x32x64_f8f6f4 v[2:17], v[42:49], v[98:105], v[2:17], v236, v236 op_sel_hi:[0,0,0]
	v_writelane_b32 v240, s21, 11
	v_writelane_b32 v240, s22, 12
	v_writelane_b32 v240, s23, 13
	s_waitcnt vmcnt(36)
	v_mfma_scale_f32_32x32x64_f8f6f4 v[2:17], v[50:57], v[106:113], v[2:17], v236, v236 op_sel_hi:[0,0,0]
	s_waitcnt vmcnt(32)
	v_mfma_scale_f32_32x32x64_f8f6f4 v[2:17], v[58:65], v[114:121], v[2:17], v236, v236 op_sel_hi:[0,0,0]
	s_lshl_b32 s0, s52, 12
	s_add_i32 s95, s95, s53
	s_or_b32 s40, s33, 1
	v_writelane_b32 v240, s0, 14
	v_lshl_or_b32 v200, v194, 2, s0
	v_cmp_eq_u32_e64 s[0:1], v163, v160
	v_cmp_eq_u32_e64 s[2:3], 1, v26
	v_cmp_eq_u32_e64 s[4:5], 2, v26
	v_cmp_eq_u32_e64 s[6:7], 3, v26
	v_cmp_eq_u32_e64 s[8:9], 8, v26
	v_cmp_eq_u32_e64 s[10:11], 9, v26
	v_cmp_eq_u32_e64 s[12:13], 10, v26
	v_cmp_eq_u32_e64 s[14:15], 11, v26
	v_cmp_eq_u32_e64 s[16:17], 16, v26
	v_cmp_eq_u32_e64 s[18:19], 17, v26
	v_cmp_eq_u32_e64 s[20:21], 18, v26
	v_cmp_eq_u32_e64 s[22:23], 19, v26
	v_cmp_eq_u32_e64 s[24:25], 24, v26
	v_cmp_eq_u32_e64 s[26:27], 25, v26
	v_cmp_eq_u32_e64 s[28:29], 26, v26
	v_cmp_eq_u32_e64 s[30:31], 27, v26
	s_mov_b32 s96, 0x3f4ccccd
	v_mov_b32_e32 v161, 0
	v_mov_b32_e32 v159, 0
	v_mov_b32_e32 v158, 0
	v_mov_b32_e32 v157, 0
	v_mov_b32_e32 v156, 0
	v_mov_b32_e32 v155, 0
	v_mov_b32_e32 v154, 0
	v_mov_b32_e32 v227, 0
	v_mov_b32_e32 v224, 0
	v_mov_b32_e32 v217, 0
	v_mov_b32_e32 v216, 0
	v_mov_b32_e32 v209, 0
	v_mov_b32_e32 v191, 0
	v_mov_b32_e32 v189, 0
	v_mov_b32_e32 v188, 0
	v_mov_b32_e32 v187, 0
	v_mov_b32_e32 v186, 0
	v_mov_b32_e32 v185, 0
	v_mov_b32_e32 v184, 0
	v_mov_b32_e32 v183, 0
	v_mov_b32_e32 v182, 0
	v_mov_b32_e32 v181, 0
	v_mov_b32_e32 v180, 0
	v_mov_b32_e32 v179, 0
	v_mov_b32_e32 v178, 0
	v_mov_b32_e32 v177, 0
	v_mov_b32_e32 v176, 0
	v_mov_b32_e32 v175, 0
	v_mov_b32_e32 v174, 0
	v_mov_b32_e32 v173, 0
	v_mov_b32_e32 v172, 0
	v_mov_b32_e32 v171, 0
	v_mov_b32_e32 v170, 0
	v_mov_b32_e32 v169, 0
	v_mov_b32_e32 v168, 0
	v_mov_b32_e32 v167, 0
	v_mov_b32_e32 v166, 0
	v_mov_b32_e32 v165, 0
	v_mov_b32_e32 v164, 0
